# v50 + P0 rmsnorm1 loop: loop-invariant gain vector loaded once before the row loop instead of a per-row serial load->vmcnt(0) ladder between the row's stores
# speedup vs baseline: 1.0194x; 1.0194x over previous
.LBB0_18:
	s_cmp_gt_i32 s24, 0xffff
	s_cbranch_scc1 .LBB0_21
	v_mbcnt_lo_u32_b32 v6, -1, 0
	v_mbcnt_hi_u32_b32 v11, -1, v6
	v_and_b32_e32 v6, 64, v11
	s_ashr_i32 s25, s24, 31
	v_add_u32_e32 v12, 64, v6
	v_xor_b32_e32 v6, 1, v11
	s_lshl_b64 s[0:1], s[24:25], 11
	v_cmp_lt_i32_e32 vcc, v6, v12
	v_xor_b32_e32 v7, 2, v11
	s_add_u32 s0, s66, s0
	v_ashrrev_i32_e32 v1, 31, v0
	v_cndmask_b32_e32 v6, v11, v6, vcc
	v_cmp_lt_i32_e32 vcc, v7, v12
	v_xor_b32_e32 v8, 4, v11
	s_addc_u32 s1, s67, s1
	v_lshlrev_b64 v[4:5], 4, v[0:1]
	v_cndmask_b32_e32 v7, v11, v7, vcc
	v_cmp_lt_i32_e32 vcc, v8, v12
	v_xor_b32_e32 v9, 8, v11
	v_lshl_add_u64 v[0:1], v[0:1], 3, s[0:1]
	s_mov_b64 s[0:1], 0xa000000
	s_ashr_i32 s7, s6, 31
	v_lshl_add_u64 v[2:3], s[10:11], 0, v[4:5]
	v_cndmask_b32_e32 v8, v11, v8, vcc
	v_cmp_lt_i32_e32 vcc, v9, v12
	v_xor_b32_e32 v10, 16, v11
	v_lshl_add_u64 v[0:1], v[0:1], 0, s[0:1]
	s_lshl_b64 s[10:11], s[6:7], 11
	s_lshl_b64 s[0:1], s[24:25], 12
	v_cndmask_b32_e32 v9, v11, v9, vcc
	v_cmp_lt_i32_e32 vcc, v10, v12
	v_xor_b32_e32 v13, 32, v11
	s_add_u32 s0, s8, s0
	v_cndmask_b32_e32 v10, v11, v10, vcc
	v_cmp_lt_i32_e32 vcc, v13, v12
	s_addc_u32 s1, s9, s1
	v_lshl_add_u64 v[4:5], s[0:1], 0, v[4:5]
	v_cndmask_b32_e32 v11, v11, v13, vcc
	s_mov_b64 s[0:1], 0xc00
	v_lshlrev_b32_e32 v6, 2, v6
	v_lshlrev_b32_e32 v7, 2, v7
	v_lshlrev_b32_e32 v8, 2, v8
	v_lshlrev_b32_e32 v9, 2, v9
	v_lshlrev_b32_e32 v10, 2, v10
	v_lshlrev_b32_e32 v11, 2, v11
	v_lshl_add_u64 v[4:5], v[4:5], 0, s[0:1]
	s_lshl_b64 s[12:13], s[6:7], 12
	v_mov_b32_e32 v12, 0x358637bd
	s_mov_b32 s3, 0xf800000
	v_mov_b32_e32 v13, 0x260
	s_movk_i32 s7, 0x7fff
	s_mov_b32 s25, 0xffff0000
	s_mov_b32 s26, s24
	global_load_dwordx4 v[174:177], v[2:3], off
	global_load_dwordx4 v[178:181], v[2:3], off offset:1024
	global_load_dwordx4 v[182:185], v[2:3], off offset:2048
	global_load_dwordx4 v[186:189], v[2:3], off offset:3072
	s_waitcnt vmcnt(0)
.LBB0_20:
	global_load_dwordx4 v[14:17], v[4:5], off offset:-3072
	global_load_dwordx4 v[18:21], v[4:5], off offset:-2048
	global_load_dwordx4 v[22:25], v[4:5], off offset:-1024
	global_load_dwordx4 v[26:29], v[4:5], off
	s_add_i32 s26, s26, s6
	v_lshl_add_u64 v[4:5], v[4:5], 0, s[12:13]
	s_cmp_gt_i32 s26, 0xffff
	s_waitcnt vmcnt(3)
	v_pk_mul_f32 v[34:35], v[16:17], v[16:17]
	v_pk_mul_f32 v[36:37], v[14:15], v[14:15]
	s_waitcnt vmcnt(2)
	v_pk_mul_f32 v[38:39], v[20:21], v[20:21]
	v_pk_mul_f32 v[40:41], v[18:19], v[18:19]
	v_pk_mov_b32 v[46:47], v[36:37], v[34:35] op_sel:[1,0]
	v_mov_b32_e32 v37, v35
	v_pk_mov_b32 v[34:35], v[40:41], v[38:39] op_sel:[1,0]
	v_mov_b32_e32 v41, v39
	s_waitcnt vmcnt(0)
	v_mul_f32_e32 v45, v26, v26
	v_mul_f32_e32 v42, v23, v23
	v_mul_f32_e32 v44, v25, v25
	v_pk_add_f32 v[36:37], v[46:47], v[36:37]
	v_pk_add_f32 v[34:35], v[34:35], v[40:41]
	v_mul_f32_e32 v48, v27, v27
	v_mul_f32_e32 v49, v28, v28
	v_mul_f32_e32 v50, v29, v29
	v_pk_fma_f32 v[38:39], v[22:23], v[22:23], v[42:43] op_sel_hi:[1,1,0]
	v_pk_fma_f32 v[42:43], v[24:25], v[24:25], v[44:45] op_sel_hi:[1,1,0]
	v_pk_add_f32 v[36:37], v[36:37], v[36:37] op_sel:[0,1] op_sel_hi:[1,0]
	v_pk_add_f32 v[34:35], v[34:35], v[34:35] op_sel:[0,1] op_sel_hi:[1,0]
	v_mov_b32_e32 v39, v49
	v_mov_b32_e32 v43, v50
	v_mov_b32_e32 v37, v45
	v_mov_b32_e32 v35, v48
	v_pk_add_f32 v[38:39], v[38:39], v[42:43]
	v_pk_add_f32 v[34:35], v[36:37], v[34:35]
	s_nop 0
	v_pk_add_f32 v[34:35], v[34:35], v[38:39]
	s_nop 0
	v_add_f32_e32 v34, v34, v35
	ds_bpermute_b32 v35, v6, v34
	s_waitcnt lgkmcnt(0)
	v_add_f32_e32 v34, v34, v35
	ds_bpermute_b32 v35, v7, v34
	s_waitcnt lgkmcnt(0)
	v_add_f32_e32 v34, v34, v35
	ds_bpermute_b32 v35, v8, v34
	s_waitcnt lgkmcnt(0)
	v_add_f32_e32 v34, v34, v35
	ds_bpermute_b32 v35, v9, v34
	s_waitcnt lgkmcnt(0)
	v_add_f32_e32 v34, v34, v35
	ds_bpermute_b32 v35, v10, v34
	s_waitcnt lgkmcnt(0)
	v_add_f32_e32 v34, v34, v35
	ds_bpermute_b32 v35, v11, v34
	s_waitcnt lgkmcnt(0)
	v_add_f32_e32 v34, v34, v35
	v_fmamk_f32 v34, v34, 0x3a800000, v12
	v_mul_f32_e32 v35, 0x4f800000, v34
	v_cmp_gt_f32_e32 vcc, s3, v34
	s_nop 1
	v_cndmask_b32_e32 v34, v34, v35, vcc
	v_sqrt_f32_e32 v35, v34
	s_nop 0
	v_add_u32_e32 v36, -1, v35
	v_add_u32_e32 v37, 1, v35
	v_fma_f32 v38, -v36, v35, v34
	v_fma_f32 v39, -v37, v35, v34
	v_cmp_ge_f32_e64 s[0:1], 0, v38
	s_nop 1
	v_cndmask_b32_e64 v35, v35, v36, s[0:1]
	v_cmp_lt_f32_e64 s[0:1], 0, v39
	s_nop 1
	v_cndmask_b32_e64 v35, v35, v37, s[0:1]
	v_mul_f32_e32 v36, 0x37800000, v35
	v_cndmask_b32_e32 v35, v35, v36, vcc
	v_cmp_class_f32_e32 vcc, v34, v13
	s_nop 1
	v_cndmask_b32_e32 v34, v35, v34, vcc
	v_div_scale_f32 v35, s[0:1], v34, v34, 1.0
	v_rcp_f32_e32 v37, v35
	v_div_scale_f32 v36, vcc, 1.0, v34, 1.0
	v_fma_f32 v38, -v35, v37, 1.0
	v_fmac_f32_e32 v37, v38, v37
	v_mul_f32_e32 v38, v36, v37
	v_fma_f32 v39, -v35, v38, v36
	v_fmac_f32_e32 v38, v39, v37
	v_fma_f32 v35, -v35, v38, v36
	v_div_fmas_f32 v35, v35, v37, v38
	v_div_fixup_f32 v34, v35, v34, 1.0
	v_pk_mul_f32 v[14:15], v[14:15], v[34:35] op_sel_hi:[1,0]
	v_pk_mul_f32 v[16:17], v[16:17], v[34:35] op_sel_hi:[1,0]
	v_pk_mul_f32 v[14:15], v[174:175], v[14:15]
	v_pk_mul_f32 v[16:17], v[176:177], v[16:17]
	v_bfe_u32 v30, v14, 16, 1
	v_bfe_u32 v32, v16, 16, 1
	v_bfe_u32 v31, v15, 16, 1
	v_bfe_u32 v33, v17, 16, 1
	v_add3_u32 v14, v14, v30, s7
	v_add3_u32 v16, v16, v32, s7
	v_add3_u32 v15, v15, v31, s7
	v_add3_u32 v17, v17, v33, s7
	v_lshrrev_b32_e32 v14, 16, v14
	v_lshrrev_b32_e32 v16, 16, v16
	v_and_or_b32 v14, v15, s25, v14
	v_and_or_b32 v15, v17, s25, v16
	global_store_dwordx2 v[0:1], v[14:15], off
	v_pk_mul_f32 v[18:19], v[18:19], v[34:35] op_sel_hi:[1,0]
	v_pk_mul_f32 v[20:21], v[20:21], v[34:35] op_sel_hi:[1,0]
	v_pk_mul_f32 v[14:15], v[178:179], v[18:19]
	v_pk_mul_f32 v[16:17], v[180:181], v[20:21]
	v_bfe_u32 v18, v14, 16, 1
	v_bfe_u32 v20, v16, 16, 1
	v_bfe_u32 v19, v15, 16, 1
	v_bfe_u32 v21, v17, 16, 1
	v_add3_u32 v14, v14, v18, s7
	v_add3_u32 v16, v16, v20, s7
	v_add3_u32 v15, v15, v19, s7
	v_add3_u32 v17, v17, v21, s7
	v_lshrrev_b32_e32 v14, 16, v14
	v_lshrrev_b32_e32 v16, 16, v16
	v_and_or_b32 v14, v15, s25, v14
	v_and_or_b32 v15, v17, s25, v16
	global_store_dwordx2 v[0:1], v[14:15], off offset:512
	v_pk_mul_f32 v[18:19], v[22:23], v[34:35] op_sel_hi:[1,0]
	v_pk_mul_f32 v[20:21], v[24:25], v[34:35] op_sel_hi:[1,0]
	v_pk_mul_f32 v[14:15], v[182:183], v[18:19]
	v_pk_mul_f32 v[16:17], v[184:185], v[20:21]
	v_bfe_u32 v18, v14, 16, 1
	v_bfe_u32 v20, v16, 16, 1
	v_bfe_u32 v19, v15, 16, 1
	v_bfe_u32 v21, v17, 16, 1
	v_add3_u32 v14, v14, v18, s7
	v_add3_u32 v16, v16, v20, s7
	v_add3_u32 v15, v15, v19, s7
	v_add3_u32 v17, v17, v21, s7
	v_lshrrev_b32_e32 v14, 16, v14
	v_lshrrev_b32_e32 v16, 16, v16
	v_and_or_b32 v14, v15, s25, v14
	v_and_or_b32 v15, v17, s25, v16
	global_store_dwordx2 v[0:1], v[14:15], off offset:1024
	v_pk_mul_f32 v[18:19], v[26:27], v[34:35] op_sel_hi:[1,0]
	v_pk_mul_f32 v[20:21], v[28:29], v[34:35] op_sel_hi:[1,0]
	v_pk_mul_f32 v[14:15], v[186:187], v[18:19]
	v_pk_mul_f32 v[16:17], v[188:189], v[20:21]
	v_bfe_u32 v18, v14, 16, 1
	v_bfe_u32 v20, v16, 16, 1
	v_bfe_u32 v19, v15, 16, 1
	v_bfe_u32 v21, v17, 16, 1
	v_add3_u32 v14, v14, v18, s7
	v_add3_u32 v16, v16, v20, s7
	v_add3_u32 v15, v15, v19, s7
	v_add3_u32 v17, v17, v21, s7
	v_lshrrev_b32_e32 v14, 16, v14
	v_lshrrev_b32_e32 v16, 16, v16
	v_and_or_b32 v14, v15, s25, v14
	v_and_or_b32 v15, v17, s25, v16
	global_store_dwordx2 v[0:1], v[14:15], off offset:1536
	v_lshl_add_u64 v[0:1], v[0:1], 0, s[10:11]
	s_cbranch_scc0 .LBB0_20
